# E3 plus: L2 warm-up load issued only by the wave that touches real lines (waves 1-3 no longer issue a dummy load)
# speedup vs baseline: 1.0130x; 1.0066x over previous
.LBB1_6:
	s_or_b64 exec, exec, s[10:11]
	v_lshrrev_b32_e32 v10, 6, v0
	v_lshlrev_b32_e32 v4, 7, v10
	v_lshrrev_b32_e32 v32, 1, v1
	v_lshl_or_b32 v71, s5, 9, v4
	v_lshl_or_b32 v68, v32, 2, v71
	v_mov_b32_e32 v69, 0
	s_waitcnt lgkmcnt(0)
	v_cmp_gt_u32_e32 vcc, 64, v0
	v_lshlrev_b32_e32 v6, 4, v1
	v_mov_b32_e32 v7, v69
	s_and_saveexec_b64 s[10:11], vcc
	s_cbranch_execz .Lwarm_skip
	global_load_dword v70, v[2:3], off
.Lwarm_skip:
	s_or_b64 exec, exec, s[10:11]
	v_mad_u64_u32 v[2:3], s[6:7], v71, 12, s[6:7]
	v_lshlrev_b32_e32 v4, 2, v71
	v_mov_b32_e32 v5, v69
	s_movk_i32 s6, 0xfe00
	v_lshl_add_u64 v[4:5], s[8:9], 0, v[4:5]
	v_lshl_add_u64 v[8:9], v[2:3], 0, v[6:7]
	s_mov_b32 s7, -1
	v_lshl_add_u64 v[4:5], v[4:5], 0, v[6:7]
	v_lshl_add_u64 v[2:3], v[8:9], 0, s[6:7]
	v_cmp_gt_u32_e32 vcc, 32, v1
	v_lshlrev_b32_e32 v33, 12, v10
	v_add_u32_e32 v34, v33, v6
	v_cndmask_b32_e32 v3, v3, v5, vcc
	v_cndmask_b32_e32 v2, v2, v4, vcc
	global_load_dwordx4 v[2:5], v[2:3], off
	v_and_b32_e32 v72, 1, v0
	v_lshl_add_u32 v0, v32, 4, v33
	v_lshlrev_b32_e32 v73, 4, v32
	v_lshlrev_b32_e32 v74, 6, v72
	v_xor_b32_e32 v73, v73, v74
	v_lshl_add_u32 v73, v72, 11, v73
	v_lshl_add_u32 v73, v10, 12, v73
	v_and_b32_e32 v74, 31, v1
	v_lshrrev_b32_e32 v75, 5, v1
	v_lshl_or_b32 v76, v74, 2, v71
	v_lshlrev_b32_e32 v74, 4, v74
	v_lshlrev_b32_e32 v77, 6, v75
	v_xor_b32_e32 v74, v74, v77
	v_lshl_add_u32 v74, v75, 11, v74
	v_lshl_add_u32 v74, v10, 12, v74
	v_lshlrev_b32_e32 v77, 7, v71
	v_and_b32_e32 v77, 0xe000000, v77
	v_and_b32_e32 v76, 0x3fffc, v76
	v_lshlrev_b32_e32 v75, 21, v75
	v_or3_b32 v75, v77, v75, v76
	v_lshlrev_b32_e32 v75, 2, v75
	s_mul_i32 s6, s4, 0x138800
	s_mul_hi_i32 s5, s4, 0x138800
	s_add_u32 s2, s2, s6
	s_addc_u32 s3, s3, s5
	global_load_dwordx4 v[28:31], v[8:9], off offset:512
	s_waitcnt vmcnt(1)
	ds_write_b128 v34, v[2:5]
	ds_read_b128 v[4:7], v0
	v_lshlrev_b32_e32 v0, 4, v72
	s_waitcnt lgkmcnt(0)
	v_max_i32_e32 v1, 0, v4
	v_max_i32_e32 v2, 0, v5
	v_max_i32_e32 v3, 0, v6
	v_max_i32_e32 v8, 0, v7
	v_lshl_or_b32 v35, v1, 7, v0
	v_lshl_or_b32 v36, v2, 7, v0
	v_lshl_or_b32 v37, v3, 7, v0
	v_lshl_or_b32 v38, v8, 7, v0
	global_load_dwordx4 v[20:23], v35, s[2:3]
	global_load_dwordx4 v[16:19], v35, s[2:3] offset:32
	global_load_dwordx4 v[8:11], v35, s[2:3] offset:64
	global_load_dwordx4 v[64:67], v36, s[2:3]
	global_load_dwordx4 v[60:63], v36, s[2:3] offset:32
	global_load_dwordx4 v[56:59], v36, s[2:3] offset:64
	global_load_dwordx4 v[52:55], v37, s[2:3]
	global_load_dwordx4 v[48:51], v37, s[2:3] offset:32
	global_load_dwordx4 v[44:47], v37, s[2:3] offset:64
	global_load_dwordx4 v[24:27], v38, s[2:3]
	global_load_dwordx4 v[12:15], v38, s[2:3] offset:32
	global_load_dwordx4 v[0:3], v38, s[2:3] offset:64
	s_waitcnt vmcnt(12)
	ds_write_b128 v34, v[28:31] offset:1024
	v_mul_u32_u24_e32 v28, 48, v32
	v_cmp_lt_i32_e32 vcc, -1, v4
	v_add_u32_e32 v31, v33, v28
	v_mov_b32_e32 v28, 0
	s_and_saveexec_b64 s[2:3], vcc
	ds_read_b32 v28, v31 offset:512
	s_or_b64 exec, exec, s[2:3]
	s_and_saveexec_b64 s[2:3], vcc
	ds_read_b32 v69, v31 offset:516
	s_or_b64 exec, exec, s[2:3]
	v_mov_b32_e32 v29, 0
	v_mov_b32_e32 v4, 0
	s_and_saveexec_b64 s[2:3], vcc
	ds_read_b32 v4, v31 offset:520
	s_or_b64 exec, exec, s[2:3]
	s_waitcnt vmcnt(11) lgkmcnt(0)
	v_fma_mix_f32 v30, v28, v20, v29 op_sel_hi:[0,1,0]
	v_fma_mix_f32 v20, v28, v20, v29 op_sel:[0,1,0] op_sel_hi:[0,1,0]
	v_fma_mix_f32 v32, v28, v21, v29 op_sel_hi:[0,1,0]
	v_fma_mix_f32 v21, v28, v21, v29 op_sel:[0,1,0] op_sel_hi:[0,1,0]
	v_fma_mix_f32 v33, v28, v22, v29 op_sel_hi:[0,1,0]
	v_fma_mix_f32 v22, v28, v22, v29 op_sel:[0,1,0] op_sel_hi:[0,1,0]
	v_fma_mix_f32 v34, v28, v23, v29 op_sel_hi:[0,1,0]
	v_fma_mix_f32 v23, v28, v23, v29 op_sel:[0,1,0] op_sel_hi:[0,1,0]
	s_waitcnt vmcnt(10)
	v_fma_mix_f32 v28, v69, v16, v30 op_sel_hi:[0,1,0]
	v_fma_mix_f32 v16, v69, v16, v20 op_sel:[0,1,0] op_sel_hi:[0,1,0]
	v_fma_mix_f32 v20, v69, v17, v32 op_sel_hi:[0,1,0]
	v_cmp_lt_i32_e32 vcc, -1, v5
	v_fma_mix_f32 v17, v69, v17, v21 op_sel:[0,1,0] op_sel_hi:[0,1,0]
	v_fma_mix_f32 v21, v69, v18, v33 op_sel_hi:[0,1,0]
	v_fma_mix_f32 v18, v69, v18, v22 op_sel:[0,1,0] op_sel_hi:[0,1,0]
	v_fma_mix_f32 v22, v69, v19, v34 op_sel_hi:[0,1,0]
	v_fma_mix_f32 v19, v69, v19, v23 op_sel:[0,1,0] op_sel_hi:[0,1,0]
	s_waitcnt vmcnt(9)
	v_fma_mix_f32 v40, v4, v8, v28 op_sel_hi:[0,1,0]
	v_fma_mix_f32 v36, v4, v8, v16 op_sel:[0,1,0] op_sel_hi:[0,1,0]
	v_fma_mix_f32 v32, v4, v9, v20 op_sel_hi:[0,1,0]
	v_fma_mix_f32 v28, v4, v9, v17 op_sel:[0,1,0] op_sel_hi:[0,1,0]
	v_fma_mix_f32 v20, v4, v10, v21 op_sel_hi:[0,1,0]
	v_fma_mix_f32 v16, v4, v10, v18 op_sel:[0,1,0] op_sel_hi:[0,1,0]
	v_fma_mix_f32 v8, v4, v11, v22 op_sel_hi:[0,1,0]
	v_fma_mix_f32 v4, v4, v11, v19 op_sel:[0,1,0] op_sel_hi:[0,1,0]
	s_and_saveexec_b64 s[2:3], vcc
	ds_read_b32 v29, v31 offset:524
	s_or_b64 exec, exec, s[2:3]
	v_mov_b32_e32 v5, 0
	v_mov_b32_e32 v9, 0
	s_and_saveexec_b64 s[2:3], vcc
	ds_read_b32 v9, v31 offset:528
	s_or_b64 exec, exec, s[2:3]
	s_and_saveexec_b64 s[2:3], vcc
	ds_read_b32 v5, v31 offset:532
	s_or_b64 exec, exec, s[2:3]
	v_mov_b32_e32 v10, 0
	s_waitcnt vmcnt(8) lgkmcnt(0)
	v_fma_mix_f32 v18, v29, v65, v10 op_sel_hi:[0,1,0]
	v_fma_mix_f32 v17, v29, v64, v10 op_sel:[0,1,0] op_sel_hi:[0,1,0]
	v_fma_mix_f32 v21, v29, v66, v10 op_sel_hi:[0,1,0]
	v_fma_mix_f32 v11, v29, v64, v10 op_sel_hi:[0,1,0]
	v_fma_mix_f32 v19, v29, v65, v10 op_sel:[0,1,0] op_sel_hi:[0,1,0]
	s_waitcnt vmcnt(7)
	v_fma_mix_f32 v18, v9, v61, v18 op_sel_hi:[0,1,0]
	v_fma_mix_f32 v22, v29, v66, v10 op_sel:[0,1,0] op_sel_hi:[0,1,0]
	v_fma_mix_f32 v23, v29, v67, v10 op_sel_hi:[0,1,0]
	v_fma_mix_f32 v29, v29, v67, v10 op_sel:[0,1,0] op_sel_hi:[0,1,0]
	v_fma_mix_f32 v17, v9, v60, v17 op_sel:[0,1,0] op_sel_hi:[0,1,0]
	v_fma_mix_f32 v21, v9, v62, v21 op_sel_hi:[0,1,0]
	s_waitcnt vmcnt(6)
	v_fma_mix_f32 v33, v5, v57, v18 op_sel_hi:[0,1,0]
	v_cmp_lt_i32_e32 vcc, -1, v6
	v_mov_b32_e32 v18, 0
	v_fma_mix_f32 v11, v9, v60, v11 op_sel_hi:[0,1,0]
	v_fma_mix_f32 v19, v9, v61, v19 op_sel:[0,1,0] op_sel_hi:[0,1,0]
	v_fma_mix_f32 v22, v9, v62, v22 op_sel:[0,1,0] op_sel_hi:[0,1,0]
	v_fma_mix_f32 v23, v9, v63, v23 op_sel_hi:[0,1,0]
	v_fma_mix_f32 v30, v9, v63, v29 op_sel:[0,1,0] op_sel_hi:[0,1,0]
	v_fma_mix_f32 v37, v5, v56, v17 op_sel:[0,1,0] op_sel_hi:[0,1,0]
	s_nop 0
	v_fma_mix_f32 v41, v5, v56, v11 op_sel_hi:[0,1,0]
	v_fma_mix_f32 v29, v5, v57, v19 op_sel:[0,1,0] op_sel_hi:[0,1,0]
	v_fma_mix_f32 v21, v5, v58, v21 op_sel_hi:[0,1,0]
	v_fma_mix_f32 v17, v5, v58, v22 op_sel:[0,1,0] op_sel_hi:[0,1,0]
	v_fma_mix_f32 v9, v5, v59, v23 op_sel_hi:[0,1,0]
	v_fma_mix_f32 v5, v5, v59, v30 op_sel:[0,1,0] op_sel_hi:[0,1,0]
	s_and_saveexec_b64 s[2:3], vcc
	ds_read_b32 v18, v31 offset:536
	s_or_b64 exec, exec, s[2:3]
	s_and_saveexec_b64 s[2:3], vcc
	ds_read_b32 v10, v31 offset:540
	s_or_b64 exec, exec, s[2:3]
	v_mov_b32_e32 v11, 0
	v_mov_b32_e32 v6, 0
	s_and_saveexec_b64 s[2:3], vcc
	ds_read_b32 v6, v31 offset:544
	s_or_b64 exec, exec, s[2:3]
	s_waitcnt vmcnt(5) lgkmcnt(0)
	v_fma_mix_f32 v22, v18, v52, v11 op_sel:[0,1,0] op_sel_hi:[0,1,0]
	v_fma_mix_f32 v30, v18, v53, v11 op_sel:[0,1,0] op_sel_hi:[0,1,0]
	v_fma_mix_f32 v19, v18, v52, v11 op_sel_hi:[0,1,0]
	v_fma_mix_f32 v23, v18, v53, v11 op_sel_hi:[0,1,0]
	v_fma_mix_f32 v34, v18, v54, v11 op_sel_hi:[0,1,0]
	v_fma_mix_f32 v35, v18, v54, v11 op_sel:[0,1,0] op_sel_hi:[0,1,0]
	v_fma_mix_f32 v38, v18, v55, v11 op_sel_hi:[0,1,0]
	v_fma_mix_f32 v18, v18, v55, v11 op_sel:[0,1,0] op_sel_hi:[0,1,0]
	s_waitcnt vmcnt(4)
	v_fma_mix_f32 v22, v10, v48, v22 op_sel:[0,1,0] op_sel_hi:[0,1,0]
	v_fma_mix_f32 v30, v10, v49, v30 op_sel:[0,1,0] op_sel_hi:[0,1,0]
	v_cmp_lt_i32_e32 vcc, -1, v7
	v_fma_mix_f32 v19, v10, v48, v19 op_sel_hi:[0,1,0]
	v_fma_mix_f32 v23, v10, v49, v23 op_sel_hi:[0,1,0]
	v_fma_mix_f32 v39, v10, v50, v34 op_sel_hi:[0,1,0]
	v_fma_mix_f32 v35, v10, v50, v35 op_sel:[0,1,0] op_sel_hi:[0,1,0]
	v_fma_mix_f32 v43, v10, v51, v38 op_sel_hi:[0,1,0]
	v_fma_mix_f32 v48, v10, v51, v18 op_sel:[0,1,0] op_sel_hi:[0,1,0]
	s_waitcnt vmcnt(3)
	v_fma_mix_f32 v42, v6, v44, v19 op_sel_hi:[0,1,0]
	v_fma_mix_f32 v38, v6, v44, v22 op_sel:[0,1,0] op_sel_hi:[0,1,0]
	v_fma_mix_f32 v34, v6, v45, v23 op_sel_hi:[0,1,0]
	v_fma_mix_f32 v30, v6, v45, v30 op_sel:[0,1,0] op_sel_hi:[0,1,0]
	v_fma_mix_f32 v22, v6, v46, v39 op_sel_hi:[0,1,0]
	v_fma_mix_f32 v18, v6, v46, v35 op_sel:[0,1,0] op_sel_hi:[0,1,0]
	v_fma_mix_f32 v10, v6, v47, v43 op_sel_hi:[0,1,0]
	v_fma_mix_f32 v6, v6, v47, v48 op_sel:[0,1,0] op_sel_hi:[0,1,0]
	s_and_saveexec_b64 s[2:3], vcc
	ds_read_b32 v11, v31 offset:548
	s_or_b64 exec, exec, s[2:3]
	s_load_dwordx2 s[0:1], s[0:1], 0x18
	s_ashr_i32 s5, s4, 31
	v_mov_b32_e32 v7, 0
	v_mov_b32_e32 v19, 0
	s_and_saveexec_b64 s[2:3], vcc
	ds_read_b32 v19, v31 offset:552
	s_or_b64 exec, exec, s[2:3]
	s_and_saveexec_b64 s[2:3], vcc
	ds_read_b32 v7, v31 offset:556
	s_or_b64 exec, exec, s[2:3]
	v_mov_b32_e32 v23, 0
	s_waitcnt vmcnt(2) lgkmcnt(0)
	v_fma_mix_f32 v31, v11, v24, v23 op_sel_hi:[0,1,0]
	v_fma_mix_f32 v24, v11, v24, v23 op_sel:[0,1,0] op_sel_hi:[0,1,0]
	v_fma_mix_f32 v35, v11, v25, v23 op_sel_hi:[0,1,0]
	v_fma_mix_f32 v25, v11, v25, v23 op_sel:[0,1,0] op_sel_hi:[0,1,0]
	v_fma_mix_f32 v39, v11, v26, v23 op_sel_hi:[0,1,0]
	v_fma_mix_f32 v26, v11, v26, v23 op_sel:[0,1,0] op_sel_hi:[0,1,0]
	v_fma_mix_f32 v43, v11, v27, v23 op_sel_hi:[0,1,0]
	v_fma_mix_f32 v11, v11, v27, v23 op_sel:[0,1,0] op_sel_hi:[0,1,0]
	s_waitcnt vmcnt(1)
	v_fma_mix_f32 v23, v19, v12, v31 op_sel_hi:[0,1,0]
	s_lshl_b64 s[2:3], s[4:5], 24
	v_fma_mix_f32 v12, v19, v12, v24 op_sel:[0,1,0] op_sel_hi:[0,1,0]
	v_fma_mix_f32 v24, v19, v13, v35 op_sel_hi:[0,1,0]
	v_fma_mix_f32 v13, v19, v13, v25 op_sel:[0,1,0] op_sel_hi:[0,1,0]
	v_fma_mix_f32 v25, v19, v14, v39 op_sel_hi:[0,1,0]
	v_fma_mix_f32 v14, v19, v14, v26 op_sel:[0,1,0] op_sel_hi:[0,1,0]
	v_fma_mix_f32 v26, v19, v15, v43 op_sel_hi:[0,1,0]
	v_fma_mix_f32 v15, v19, v15, v11 op_sel:[0,1,0] op_sel_hi:[0,1,0]
	s_add_u32 s0, s0, s2
	s_addc_u32 s1, s1, s3
	s_add_u32 s2, s0, 0x100000
	s_addc_u32 s3, s1, 0
	s_add_u32 s4, s0, 0x200000
	s_addc_u32 s5, s1, 0
	s_add_u32 s6, s0, 0x300000
	s_addc_u32 s7, s1, 0
	s_add_u32 s8, s0, 0x400000
	s_addc_u32 s9, s1, 0
	s_add_u32 s10, s0, 0x500000
	s_addc_u32 s11, s1, 0
	s_add_u32 s12, s0, 0x600000
	s_addc_u32 s13, s1, 0
	s_add_u32 s14, s0, 0x700000
	s_addc_u32 s15, s1, 0
	s_waitcnt vmcnt(0)
	v_fma_mix_f32 v43, v7, v0, v23 op_sel_hi:[0,1,0]
	v_fma_mix_f32 v23, v7, v2, v25 op_sel_hi:[0,1,0]
	v_fma_mix_f32 v19, v7, v2, v14 op_sel:[0,1,0] op_sel_hi:[0,1,0]
	v_fma_mix_f32 v39, v7, v0, v12 op_sel:[0,1,0] op_sel_hi:[0,1,0]
	v_fma_mix_f32 v35, v7, v1, v24 op_sel_hi:[0,1,0]
	v_fma_mix_f32 v31, v7, v1, v13 op_sel:[0,1,0] op_sel_hi:[0,1,0]
	v_fma_mix_f32 v11, v7, v3, v26 op_sel_hi:[0,1,0]
	v_fma_mix_f32 v7, v7, v3, v15 op_sel:[0,1,0] op_sel_hi:[0,1,0]
	ds_write_b128 v73, v[40:43]
	ds_write_b128 v73, v[36:39] offset:512
	ds_write_b128 v73, v[32:35] offset:1024
	ds_write_b128 v73, v[28:31] offset:1536
	ds_read_b128 v[44:47], v74
	ds_read_b128 v[48:51], v74 offset:512
	ds_read_b128 v[52:55], v74 offset:1024
	ds_read_b128 v[56:59], v74 offset:1536
	ds_write_b128 v73, v[20:23]
	ds_write_b128 v73, v[16:19] offset:512
	ds_write_b128 v73, v[8:11] offset:1024
	ds_write_b128 v73, v[4:7] offset:1536
	s_waitcnt lgkmcnt(7)
	global_store_dwordx4 v75, v[44:47], s[0:1] nt
	s_waitcnt lgkmcnt(6)
	global_store_dwordx4 v75, v[48:51], s[2:3] nt
	s_waitcnt lgkmcnt(5)
	global_store_dwordx4 v75, v[52:55], s[4:5] nt
	s_waitcnt lgkmcnt(4)
	global_store_dwordx4 v75, v[56:59], s[6:7] nt
	ds_read_b128 v[60:63], v74
	ds_read_b128 v[64:67], v74 offset:512
	ds_read_b128 v[0:3], v74 offset:1024
	ds_read_b128 v[12:15], v74 offset:1536
	s_waitcnt lgkmcnt(3)
	global_store_dwordx4 v75, v[60:63], s[8:9] nt
	s_waitcnt lgkmcnt(2)
	global_store_dwordx4 v75, v[64:67], s[10:11] nt
	s_waitcnt lgkmcnt(1)
	global_store_dwordx4 v75, v[0:3], s[12:13] nt
	s_waitcnt lgkmcnt(0)
	global_store_dwordx4 v75, v[12:15], s[14:15] nt
	s_endpgm
